# plus: stream-B tile: ALiBi/bias start values via one extra MFMA k-step instead of 33 VALU fmas, row sums with v_pk_add, loop-invariant LDS address sums
# speedup vs baseline: 1.3057x; 1.0077x over previous
; __device__ __forceinline__ void att_unit_mfma(KArgs args, int b, int qb, LAS unsigned char* lds, int wave0, int lane0, int tid0) {
;     ...
;         { ATT_IDS
;         const unsigned mlo = maskw[tl * 2], mhi = maskw[tl * 2 + 1];
;         unsigned long long un = ((unsigned long long)unionw[1] << 32) | unionw[0];
;         const char* ksb = (const char*)(z + (size_t)(b * SEQ) * ZP + ZC_KS + g * 64);
;         att_state_reset(st);
;         int jq[4];
; #pragma unroll
;         for (int p = 0; p < 4; ++p) { if (un) { jq[p] = 63 - __builtin_clzll(un); un &= ~(1ull << jq[p]); } else jq[p] = -1; }
;         int jlast = jq[0];
; #pragma unroll
;         for (int p = 0; p < 3; ++p) { if (jq[p] >= 0) jlast = jq[p]; if (p == 2) { const char* kp_ = ksb + (size_t)(64 * jlast) * ZPB; att_stage(lds, p, kp_, kp_ + (ZC_VS - ZC_KS) * 2, ZPB, wave, lane); } }
;         f32x16 Sa, Sb;
; #pragma unroll 1
;         for (int i = 0; jq[0] >= 0; ++i) {
.LBB0_610:
	s_or_b64 exec, exec, s[4:5]
	s_add_i32 s1, 0, 0x24700
	v_mov_b32_e32 v142, v174
	s_mov_b32 s10, s69
	v_mov_b32_e32 v1, s1
	s_waitcnt lgkmcnt(0)
	s_barrier
	ds_read_b64 v[4:5], v1
	v_and_b32_e32 v2, 31, v142
	s_lshl_b32 s0, s10, 5
	v_and_or_b32 v141, s0, 32, v2
	v_lshl_add_u32 v1, v141, 3, 0
	s_waitcnt lgkmcnt(0)
	v_readfirstlane_b32 s0, v4
	v_readfirstlane_b32 s1, v5
	s_flbit_i32_b64 s4, s[0:1]
	s_xor_b32 s76, s4, 63
	s_lshl_b64 s[4:5], 1, s76
	s_andn2_b64 s[6:7], s[0:1], s[4:5]
	s_cmp_lg_u64 s[0:1], 0
	s_flbit_i32_b64 s0, s[6:7]
	s_cselect_b32 s12, s76, -1
	s_xor_b32 s0, s0, 63
	s_lshl_b64 s[4:5], 1, s0
	s_andn2_b64 s[4:5], s[6:7], s[4:5]
	s_lshl_b32 s8, s10, 10
	s_flbit_i32_b64 s1, s[4:5]
	s_add_i32 s86, s8, 0
	s_xor_b32 s1, s1, 63
	s_add_i32 s13, s86, 0x8000
	s_add_i32 s14, s86, 0xa000
	s_cmp_eq_u64 s[6:7], 0
	s_cselect_b64 s[6:7], -1, 0
	s_and_b64 s[8:9], s[6:7], exec
	s_cselect_b32 s15, s12, s0
	s_cmp_eq_u64 s[4:5], 0
	s_cselect_b64 s[8:9], -1, 0
	v_ashrrev_i32_e32 v4, 3, v142
	v_lshl_add_u32 v3, s10, 3, v4
	s_and_b64 s[10:11], s[8:9], exec
	s_cselect_b32 s87, s15, s1
	s_lshl_b32 s10, s87, 6
	s_mul_i32 s11, s87, 0x50000
	v_and_b32_e32 v5, 7, v142
	v_lshrrev_b32_e32 v6, 1, v3
	v_lshlrev_b32_e32 v4, 1, v4
	s_mul_hi_i32 s15, s10, 0x1400
	s_add_u32 s10, s70, s11
	v_xor_b32_e32 v6, v6, v142
	v_bitop3_b32 v4, v4, v5, 6 bitop3:0x6c
	s_addc_u32 s11, s71, s15
	v_lshlrev_b32_e32 v6, 4, v6
	v_lshlrev_b32_e32 v106, 4, v4
	v_mov_b64_e32 v[4:5], s[10:11]
	v_add_u32_e32 v1, 0x24500, v1
	v_and_b32_e32 v104, 0x70, v6
	v_mov_b32_e32 v105, v0
	v_mad_i64_i32 v[4:5], s[10:11], v3, s88, v[4:5]
	ds_read_b64 v[102:103], v1
	v_mov_b32_e32 v107, v0
	v_lshl_add_u64 v[6:7], v[4:5], 0, v[104:105]
	v_lshl_add_u64 v[6:7], v[6:7], 0, s[80:81]
	v_lshl_add_u64 v[4:5], v[4:5], 0, v[106:107]
	s_mov_b32 s10, m0
	s_mov_b32 m0, s13
	s_nop 0
	global_load_lds_dwordx4 v[6:7], off
	s_mov_b32 m0, s10
	v_lshl_add_u64 v[4:5], v[4:5], 0, s[96:97]
	s_mov_b32 s10, m0
	s_mov_b32 m0, s14
	s_nop 0
	global_load_lds_dwordx4 v[4:5], off
	s_mov_b32 m0, s10
	v_ashrrev_i32_e32 v1, 5, v142
	s_mov_b32 s84, 0
	s_cmp_lt_i32 s12, 0
	v_lshlrev_b32_e32 v100, 2, v1
	s_cbranch_scc1 .LBB0_623
	v_lshlrev_b32_e32 v143, 7, v2
	v_lshrrev_b32_e32 v2, 1, v142
	v_mad_i64_i32 v[4:5], s[10:11], v3, s88, 0
	v_bitop3_b32 v3, v2, v1, 7 bitop3:0x6c
	v_lshlrev_b32_e32 v144, 4, v3
	v_add_u32_e32 v3, 2, v1
	v_bitop3_b32 v3, v3, v2, 7 bitop3:0x78
	v_lshlrev_b32_e32 v145, 4, v3
	v_add_u32_e32 v3, 4, v1
	v_bitop3_b32 v3, v3, v2, 7 bitop3:0x78
	v_lshlrev_b32_e32 v146, 4, v3
	v_cvt_f32_i32_e32 v3, v100
	s_and_b64 s[8:9], s[8:9], exec
	s_cselect_b32 s77, -1, s1
	s_and_b64 s[6:7], s[6:7], exec
	s_cselect_b32 s85, -1, s0
	s_lshl_b64 s[0:1], 1, s1
	s_andn2_b64 s[0:1], s[4:5], s[0:1]
	v_add_u32_e32 v6, 6, v1
	v_mul_f32_e32 v148, v177, v3
	v_lshlrev_b32_e32 v3, 3, v142
	s_flbit_i32_b64 s4, s[0:1]
	v_bitop3_b32 v2, v6, v2, 7 bitop3:0x78
	v_and_b32_e32 v151, 8, v3
	v_lshrrev_b32_e32 v3, 3, v142
	v_bfe_u32 v6, v142, 1, 1
	s_xor_b32 s6, s4, 63
	v_lshlrev_b32_e32 v147, 4, v2
	v_bfe_u32 v2, v142, 2, 2
	v_and_or_b32 v3, v3, 2, v6
	s_lshl_b64 s[4:5], 1, s6
	v_lshlrev_b32_e32 v150, 7, v2
	v_lshlrev_b32_e32 v2, 5, v2
	v_lshlrev_b32_e32 v3, 4, v3
	s_andn2_b64 s[72:73], s[0:1], s[4:5]
	v_xor_b32_e32 v152, v3, v2
	v_bitop3_b32 v153, v3, v2, 64 bitop3:0x36
	v_sub_u32_e32 v2, v141, v100
	s_cmp_lg_u64 s[0:1], 0
	v_cmp_lt_i32_e32 vcc, 0, v2
	v_cmp_lt_i32_e64 s[10:11], -1, v1
	s_cselect_b32 s0, s6, -1
	s_and_b64 s[6:7], s[10:11], vcc
	v_cmp_lt_i32_e32 vcc, 1, v2
	s_and_b64 s[8:9], s[10:11], vcc
	v_cmp_lt_i32_e32 vcc, 2, v2
	s_and_b64 s[10:11], s[10:11], vcc
	v_cmp_lt_i32_e32 vcc, 7, v2
	v_cmp_lt_i32_e64 s[18:19], -3, v1
	s_and_b64 s[12:13], s[18:19], vcc
	v_cmp_lt_i32_e32 vcc, 8, v2
	v_writelane_b32 v255, s16, 59
	s_and_b64 s[14:15], s[18:19], vcc
	v_cmp_lt_i32_e32 vcc, 9, v2
	v_writelane_b32 v255, s17, 60
	s_and_b64 s[16:17], s[18:19], vcc
	v_cmp_lt_i32_e32 vcc, 10, v2
	s_and_b64 s[18:19], s[18:19], vcc
	v_cmp_lt_i32_e32 vcc, 15, v2
	v_cmp_lt_i32_e64 s[26:27], -5, v1
	s_and_b64 s[20:21], s[26:27], vcc
	v_cmp_lt_i32_e32 vcc, 16, v2
	s_and_b64 s[22:23], s[26:27], vcc
	v_cmp_lt_i32_e32 vcc, 17, v2
	s_and_b64 s[24:25], s[26:27], vcc
	v_cmp_lt_i32_e32 vcc, 18, v2
	s_and_b64 s[26:27], s[26:27], vcc
	v_cmp_lt_i32_e32 vcc, 23, v2
	v_cmp_lt_i32_e64 s[36:37], -7, v1
	s_and_b64 s[28:29], s[36:37], vcc
	v_cmp_lt_i32_e32 vcc, 24, v2
	s_and_b64 s[30:31], s[36:37], vcc
	v_cmp_lt_i32_e32 vcc, 25, v2
	s_and_b64 s[34:35], s[36:37], vcc
	v_cmp_lt_i32_e32 vcc, 26, v2
	s_and_b64 s[36:37], s[36:37], vcc
	v_cmp_lt_i32_e32 vcc, 31, v2
	v_cmp_lt_i32_e64 s[44:45], -9, v1
	s_and_b64 s[38:39], s[44:45], vcc
	v_cmp_lt_i32_e32 vcc, 32, v2
	s_and_b64 s[40:41], s[44:45], vcc
	v_cmp_lt_i32_e32 vcc, 33, v2
	s_and_b64 s[42:43], s[44:45], vcc
	v_cmp_lt_i32_e32 vcc, 34, v2
	s_and_b64 s[44:45], s[44:45], vcc
	v_cmp_lt_i32_e32 vcc, 39, v2
	v_cmp_lt_i32_e64 s[52:53], -11, v1
	s_mov_b32 s79, s46
	s_and_b64 s[46:47], s[52:53], vcc
	v_cmp_lt_i32_e32 vcc, 40, v2
	s_and_b64 s[48:49], s[52:53], vcc
	v_cmp_lt_i32_e32 vcc, 41, v2
	s_and_b64 s[50:51], s[52:53], vcc
	v_cmp_lt_i32_e32 vcc, 42, v2
	s_and_b64 s[52:53], s[52:53], vcc
	v_cmp_lt_i32_e32 vcc, 47, v2
	v_cmp_lt_i32_e64 s[60:61], -13, v1
	s_and_b64 s[54:55], s[60:61], vcc
	v_cmp_lt_i32_e32 vcc, 48, v2
	s_and_b64 s[56:57], s[60:61], vcc
	v_cmp_lt_i32_e32 vcc, 49, v2
	s_and_b64 s[58:59], s[60:61], vcc
	v_cmp_lt_i32_e32 vcc, 50, v2
	s_and_b64 s[60:61], s[60:61], vcc
	v_cmp_lt_i32_e32 vcc, 55, v2
	v_cmp_lt_i32_e64 s[68:69], -15, v1
	s_and_b64 s[62:63], s[68:69], vcc
	v_cmp_lt_i32_e32 vcc, 56, v2
	v_or_b32_e32 v3, v2, v1
; #define LAS __attribute__((address_space(3)))
; #define ATT_WAIT_BAR_PD() asm volatile("s_waitcnt vmcnt(4) lgkmcnt(0)\n\ts_barrier" ::: "memory")
; __device__ __forceinline__ void att_qk64(const LAS unsigned char* Kb, const bf16x8 (&qf)[4], float sF, float cb, int rq, int h, f32x16& S0, f32x16& S1) {
;     ...
;     const float base = cb + sF * (float)(4 * h);
; #pragma unroll
;     for (int i = 0; i < 16; ++i) { float t0 = fmaf(sF, (float)CI_(i), base); asm volatile("" : "+v"(t0)); S0[i] = t0; float t1 = fmaf(sF, (float)(CI_(i) + 32), base); asm volatile("" : "+v"(t1)); S1[i] = t1; }
;     __builtin_amdgcn_sched_barrier(0);
; #pragma unroll
;     for (int s4 = 0; s4 < 4; ++s4) { S0 = __builtin_amdgcn_mfma_f32_32x32x16_bf16(kf[0][s4], qf[s4], S0, 0, 0, 0); S1 = __builtin_amdgcn_mfma_f32_32x32x16_bf16(kf[1][s4], qf[s4], S1, 0, 0, 0); }
; __device__ __forceinline__ void att_unit_mfma(KArgs args, int b, int qb, LAS unsigned char* lds, int wave0, int lane0, int tid0) {
;     ...
;         const char* ksb = (const char*)(z + (size_t)(b * SEQ) * ZP + ZC_KS + g * 64);
;         att_state_reset(st);
;         int jq[4];
; #pragma unroll
;         for (int p = 0; p < 4; ++p) { if (un) { jq[p] = 63 - __builtin_clzll(un); un &= ~(1ull << jq[p]); } else jq[p] = -1; }
;         int jlast = jq[0];
; #pragma unroll
;         for (int p = 0; p < 3; ++p) { if (jq[p] >= 0) jlast = jq[p]; if (p == 2) { const char* kp_ = ksb + (size_t)(64 * jlast) * ZPB; att_stage(lds, p, kp_, kp_ + (ZC_VS - ZC_KS) * 2, ZPB, wave, lane); } }
;         f32x16 Sa, Sb;
; #pragma unroll 1
;         for (int i = 0; jq[0] >= 0; ++i) {
;             ATT_WAIT_BAR_PD();
;             { if (jq[3] >= 0) jlast = jq[3]; const char* kp_ = ksb + (size_t)(64 * jlast) * ZPB; att_stage(lds, (i + 3) & 3, kp_, kp_ + (ZC_VS - ZC_KS) * 2, ZPB, wave, lane); }
;             const LAS unsigned char* Kb = lds + (i & 3) * 16384; const LAS unsigned char* Vb = Kb + 8192;
;             const int j = jq[0];
;             const bool bit = ((j < 32 ? (mlo >> j) : (mhi >> (j - 32))) & 1u) != 0u;
;             att_qk64(Kb, qf, slope2, bit ? slope2 * (float)(64 * j) - st.m : -__builtin_inff(), rq, h, Sa, Sb);
;             att_softmax_pv64<false>(j == qb, Vb, -1, tl, Sa, Sb, st, h, lane);
	s_and_b64 s[64:65], s[68:69], vcc
	v_cmp_lt_i32_e32 vcc, 57, v2
	v_mov_b32_e32 v14, v0
	v_mov_b32_e32 v15, v0
	v_lshlrev_b32_e32 v149, 9, v1
	v_cmp_lt_i32_e64 s[4:5], -1, v3
	s_and_b64 s[66:67], s[68:69], vcc
	v_cmp_lt_i32_e32 vcc, 58, v2
	v_lshl_add_u64 v[108:109], s[70:71], 0, v[4:5]
	v_mov_b32_e32 v1, v0
	v_mov_b32_e32 v2, v0
	v_mov_b32_e32 v3, v0
	v_mov_b32_e32 v4, v0
	v_mov_b32_e32 v5, v0
	v_mov_b32_e32 v6, v0
	v_mov_b32_e32 v7, v0
	v_mov_b32_e32 v8, v0
	v_mov_b32_e32 v9, v0
	v_mov_b32_e32 v10, v0
	v_mov_b32_e32 v11, v0
	v_mov_b32_e32 v12, v0
	v_mov_b32_e32 v13, v0
	v_mov_b64_e32 v[30:31], v[14:15]
	v_mov_b64_e32 v[46:47], v[14:15]
	s_and_b64 s[68:69], s[68:69], vcc
	s_mov_b64 s[90:91], -1
	v_mov_b32_e32 v154, 0
	v_mov_b64_e32 v[28:29], v[12:13]
	v_mov_b64_e32 v[26:27], v[10:11]
	v_mov_b64_e32 v[24:25], v[8:9]
	v_mov_b64_e32 v[22:23], v[6:7]
	v_mov_b64_e32 v[20:21], v[4:5]
	v_mov_b64_e32 v[18:19], v[2:3]
	v_mov_b64_e32 v[16:17], v[0:1]
	v_mov_b64_e32 v[44:45], v[12:13]
	v_mov_b64_e32 v[42:43], v[10:11]
	v_mov_b64_e32 v[40:41], v[8:9]
	v_mov_b64_e32 v[38:39], v[6:7]
	v_mov_b64_e32 v[36:37], v[4:5]
	v_mov_b64_e32 v[34:35], v[2:3]
	v_mov_b64_e32 v[32:33], v[0:1]
	v_mov_b32_e32 v1, 0
	v_and_b32_e32 v14, 31, v142
	v_cvt_f32_u32_e32 v14, v14
	v_cmp_gt_u32_e32 vcc, 32, v142
	v_add_f32_e32 v15, 0x42000000, v14
	v_cvt_pk_bf16_f32 v232, v14, v14
	v_cvt_pk_bf16_f32 v236, v15, v15
	v_mov_b32_e32 v233, 0x3f803f80
	v_mov_b32_e32 v219, 0xff80
	v_cndmask_b32_e32 v232, 0, v232, vcc
	v_cndmask_b32_e32 v236, 0, v236, vcc
	v_cndmask_b32_e32 v233, 0, v233, vcc
	v_cndmask_b32_e32 v219, 0, v219, vcc
	v_cndmask_b32_e64 v244, 0, -1, vcc
	v_mov_b32_e32 v237, v233
	v_mov_b32_e32 v234, 0
	v_mov_b32_e32 v235, 0
	v_mov_b32_e32 v238, 0
	v_mov_b32_e32 v239, 0
	v_mov_b32_e32 v242, 0
	v_mov_b32_e32 v243, 0
	v_cvt_pk_bf16_f32 v14, v177, v177
	v_lshlrev_b32_e32 v14, 16, v14
	v_sub_f32_e32 v14, v177, v14
	v_cvt_pk_bf16_f32 v240, v177, v14
	v_and_b32_e32 v240, v244, v240
	v_add_u32_e32 v245, v143, v144
	v_add_u32_e32 v246, v143, v145
	v_add_u32_e32 v247, v143, v146
	v_add_u32_e32 v248, v143, v147
	v_add3_u32 v249, v149, v150, v151
	v_add_u32_e32 v220, v249, v153
	v_add_u32_e32 v249, v249, v152
	v_lshl_add_u64 v[250:251], v[108:109], 0, v[104:105]
	v_lshl_add_u64 v[250:251], v[250:251], 0, s[80:81]
	v_lshl_add_u64 v[252:253], v[108:109], 0, v[106:107]
	v_lshl_add_u64 v[252:253], v[252:253], 0, s[96:97]
.LBB0_612:
	s_cmp_lt_i32 s0, 0
	s_cselect_b32 s87, s87, s0
	s_lshl_b32 s70, s87, 6
	s_mul_i32 s70, s70, 0x1400
	s_mov_b32 s71, 0
	s_waitcnt vmcnt(4) lgkmcnt(0)
	s_barrier
	v_lshl_add_u64 v[4:5], v[250:251], 0, s[70:71]
	v_lshl_add_u64 v[2:3], v[252:253], 0, s[70:71]
	s_add_i32 s70, s84, 0xc000
	s_and_b32 s70, s70, 0xc000
	s_add_i32 s70, s86, s70
	s_mov_b32 s1, s85
	s_mov_b32 s85, s77
	s_add_i32 s71, s70, 0x2000
	s_mov_b32 s77, m0
	s_mov_b32 m0, s70
	s_nop 0
	global_load_lds_dwordx4 v[4:5], off
	s_mov_b32 m0, s77
	s_mov_b32 s70, m0
	s_mov_b32 m0, s71
	s_nop 0
	global_load_lds_dwordx4 v[2:3], off
	s_mov_b32 m0, s70
	s_lshl_b32 s71, s76, 6
	v_cvt_f32_u32_e32 v3, s71
	s_lshl_b64 s[70:71], 1, s76
	s_waitcnt lgkmcnt(0)
	v_and_b32_e32 v2, s70, v102
	v_and_or_b32 v2, v103, s71, v2
	v_fma_f32 v3, v177, v3, -v154
	v_cmp_ne_u32_e32 vcc, 0, v2
	v_cvt_pk_bf16_f32 v4, v3, v3
	v_lshlrev_b32_e32 v4, 16, v4
	v_sub_f32_e32 v4, v3, v4
	v_cvt_pk_bf16_f32 v4, v3, v4
	v_and_b32_e32 v4, v244, v4
	v_cndmask_b32_e32 v241, v219, v4, vcc
	s_and_b32 s70, s84, 0xc000
	s_add_i32 s70, s70, 0
	v_add_u32_e32 v6, s70, v245
	v_add_u32_e32 v15, s70, v246
	v_add_u32_e32 v48, s70, v247
	v_add_u32_e32 v49, s70, v248
	v_mfma_f32_32x32x16_bf16 v[64:79], v[232:235], v[240:243], 0
	ds_read_b128 v[2:5], v6
	ds_read_b128 v[6:9], v6 offset:4096
	ds_read_b128 v[10:13], v15
	ds_read_b128 v[80:83], v15 offset:4096
	ds_read_b128 v[84:87], v48
	ds_read_b128 v[88:91], v48 offset:4096
	ds_read_b128 v[92:95], v49
	ds_read_b128 v[96:99], v49 offset:4096
	v_mfma_f32_32x32x16_bf16 v[48:63], v[236:239], v[240:243], 0
	s_waitcnt lgkmcnt(7)
	v_mfma_f32_32x32x16_bf16 v[64:79], v[2:5], v[112:115], v[64:79]
	s_waitcnt lgkmcnt(6)
	v_mfma_f32_32x32x16_bf16 v[48:63], v[6:9], v[112:115], v[48:63]
	s_waitcnt lgkmcnt(5)
	v_mfma_f32_32x32x16_bf16 v[64:79], v[10:13], v[116:119], v[64:79]
	s_waitcnt lgkmcnt(4)
	v_mfma_f32_32x32x16_bf16 v[48:63], v[80:83], v[116:119], v[48:63]
	s_waitcnt lgkmcnt(3)
	v_mfma_f32_32x32x16_bf16 v[64:79], v[84:87], v[120:123], v[64:79]
	s_waitcnt lgkmcnt(2)
	v_mfma_f32_32x32x16_bf16 v[48:63], v[88:91], v[120:123], v[48:63]
	s_waitcnt lgkmcnt(1)
	v_mfma_f32_32x32x16_bf16 v[64:79], v[92:95], v[124:127], v[64:79]
	s_waitcnt lgkmcnt(0)
	v_mfma_f32_32x32x16_bf16 v[48:63], v[96:99], v[124:127], v[48:63]
	v_add_u32_e32 v4, s70, v249
	v_add_u32_e32 v12, s70, v220
	ds_read_b64_tr_b16 v[88:89], v4 offset:8192
	ds_read_b64_tr_b16 v[90:91], v4 offset:9216
	ds_read_b64_tr_b16 v[80:81], v4 offset:10240
	ds_read_b64_tr_b16 v[82:83], v4 offset:11264
	ds_read_b64_tr_b16 v[6:7], v4 offset:12288
	ds_read_b64_tr_b16 v[8:9], v4 offset:13312
	ds_read_b64_tr_b16 v[2:3], v4 offset:14336
	ds_read_b64_tr_b16 v[4:5], v4 offset:15360
	ds_read_b64_tr_b16 v[96:97], v12 offset:8192
	ds_read_b64_tr_b16 v[98:99], v12 offset:9216
	ds_read_b64_tr_b16 v[92:93], v12 offset:10240
	ds_read_b64_tr_b16 v[94:95], v12 offset:11264
	ds_read_b64_tr_b16 v[84:85], v12 offset:12288
	ds_read_b64_tr_b16 v[86:87], v12 offset:13312
	ds_read_b64_tr_b16 v[10:11], v12 offset:14336
	ds_read_b64_tr_b16 v[12:13], v12 offset:15360
	s_cmp_lg_u32 s76, s2
	s_cbranch_scc1 .LBB0_614
	v_cndmask_b32_e64 v64, v213, v64, s[4:5]
	v_cndmask_b32_e64 v65, v213, v65, s[6:7]
	v_cndmask_b32_e64 v66, v213, v66, s[8:9]
	v_cndmask_b32_e64 v67, v213, v67, s[10:11]
	v_cndmask_b32_e64 v68, v213, v68, s[12:13]
	v_cndmask_b32_e64 v69, v213, v69, s[14:15]
	v_cndmask_b32_e64 v70, v213, v70, s[16:17]
	v_cndmask_b32_e64 v71, v213, v71, s[18:19]
	v_cndmask_b32_e64 v72, v213, v72, s[20:21]
	v_cndmask_b32_e64 v73, v213, v73, s[22:23]
	v_cndmask_b32_e64 v74, v213, v74, s[24:25]
	v_cndmask_b32_e64 v75, v213, v75, s[26:27]
	v_cndmask_b32_e64 v76, v213, v76, s[28:29]
	v_cndmask_b32_e64 v77, v213, v77, s[30:31]
	v_cndmask_b32_e64 v78, v213, v78, s[34:35]
	v_cndmask_b32_e64 v79, v213, v79, s[36:37]
	v_cndmask_b32_e64 v48, v213, v48, s[38:39]
	v_cndmask_b32_e64 v49, v213, v49, s[40:41]
	v_cndmask_b32_e64 v50, v213, v50, s[42:43]
	v_cndmask_b32_e64 v51, v213, v51, s[44:45]
	v_cndmask_b32_e64 v52, v213, v52, s[46:47]
	v_cndmask_b32_e64 v53, v213, v53, s[48:49]
	v_cndmask_b32_e64 v54, v213, v54, s[50:51]
	v_cndmask_b32_e64 v55, v213, v55, s[52:53]
	v_cndmask_b32_e64 v56, v213, v56, s[54:55]
	v_cndmask_b32_e64 v57, v213, v57, s[56:57]
	v_cndmask_b32_e64 v58, v213, v58, s[58:59]
	v_cndmask_b32_e64 v59, v213, v59, s[60:61]
	v_cndmask_b32_e64 v60, v213, v60, s[62:63]
	v_cndmask_b32_e64 v61, v213, v61, s[64:65]
	v_cndmask_b32_e64 v62, v213, v62, s[66:67]
	v_cndmask_b32_e64 v63, v213, v63, s[68:69]

; __device__ __forceinline__ unsigned cvtpk(float lo, float hi) { f32x2_t v = {lo, hi}; bf16x2_t b = __builtin_convertvector(v, bf16x2_t); return __builtin_bit_cast(unsigned, b); }
;     ...
;     float ps = 0.f, pt = 0.f;
; #pragma unroll
;     for (int i = 0; i < 16; ++i) { S0[i] = __builtin_amdgcn_exp2f(S0[i]); S1[i] = __builtin_amdgcn_exp2f(S1[i]); ps += S0[i]; asm volatile("" : "+v"(ps)); pt += S1[i]; asm volatile("" : "+v"(pt)); }
;     st.l += ps + pt;
;     if (IMP) {
;         float prev3 = 0.f; const int partner = (lane ^ 32) << 2;
; #pragma unroll
;         for (int f = 0; f < 8; ++f) { const f32x16& S_ = (f >> 2) ? S1 : S0; const int q4 = f & 3; const float p3 = S_[4 * q4 + 3];
;             const float own = 2.f * (S_[4 * q4] + S_[4 * q4 + 1] + S_[4 * q4 + 2]) + p3;
;             const float inc = __builtin_bit_cast(float, __builtin_amdgcn_ds_bpermute(partner, __builtin_bit_cast(int, h ? prev3 : p3)));
;             irow[16 * ct + 2 * f + h] = own + inc;
;             prev3 = p3; }
;         if (h && ct < 3) __hip_atomic_fetch_add(irow + 16 * ct + 16, prev3, __ATOMIC_RELAXED, __HIP_MEMORY_SCOPE_WORKGROUP); }
;     u32x4 pk[4];
; #pragma unroll
;     for (int s2 = 0; s2 < 2; ++s2) { pk[s2].x = cvtpk(S0[8 * s2], S0[8 * s2 + 1]); pk[s2].y = cvtpk(S0[8 * s2 + 2], S0[8 * s2 + 3]); pk[s2].z = cvtpk(S0[8 * s2 + 4], S0[8 * s2 + 5]); pk[s2].w = cvtpk(S0[8 * s2 + 6], S0[8 * s2 + 7]);
;         pk[2 + s2].x = cvtpk(S1[8 * s2], S1[8 * s2 + 1]); pk[2 + s2].y = cvtpk(S1[8 * s2 + 2], S1[8 * s2 + 3]); pk[2 + s2].z = cvtpk(S1[8 * s2 + 4], S1[8 * s2 + 5]); pk[2 + s2].w = cvtpk(S1[8 * s2 + 6], S1[8 * s2 + 7]); }
;     __builtin_amdgcn_sched_barrier(0);
; #pragma unroll
;     for (int ks = 0; ks < 4; ++ks)
; #pragma unroll
;         for (int dt = 0; dt < 2; ++dt) st.O[dt] = __builtin_amdgcn_mfma_f32_32x32x16_bf16(vf[dt][ks], __builtin_bit_cast(bf16x8, pk[ks]), st.O[dt], 0, 0, 0);
;     __builtin_amdgcn_sched_barrier(0);
; __device__ __forceinline__ void att_unit_mfma(KArgs args, int b, int qb, LAS unsigned char* lds, int wave0, int lane0, int tid0) {
;     ...
;             jq[0] = jq[1]; jq[1] = jq[2]; jq[2] = jq[3];
;             if (un) { jq[3] = 63 - __builtin_clzll(un); un &= ~(1ull << jq[3]); } else jq[3] = -1;
;         }
.LBB0_620:
	v_exp_f32_e32 v64, v64
	v_exp_f32_e32 v65, v65
	v_exp_f32_e32 v48, v48
	v_exp_f32_e32 v49, v49
	v_exp_f32_e32 v66, v66
	v_exp_f32_e32 v67, v67
	v_pk_add_f32 v[14:15], v[64:65], v[48:49]
	v_exp_f32_e32 v50, v50
	v_exp_f32_e32 v51, v51
	v_pk_add_f32 v[14:15], v[14:15], v[66:67]
	v_exp_f32_e32 v68, v68
	v_exp_f32_e32 v69, v69
	v_pk_add_f32 v[14:15], v[14:15], v[50:51]
	v_exp_f32_e32 v52, v52
	v_exp_f32_e32 v53, v53
	v_pk_add_f32 v[14:15], v[14:15], v[68:69]
	v_exp_f32_e32 v70, v70
	v_exp_f32_e32 v71, v71
	v_pk_add_f32 v[14:15], v[14:15], v[52:53]
	v_exp_f32_e32 v54, v54
	v_exp_f32_e32 v55, v55
	v_pk_add_f32 v[14:15], v[14:15], v[70:71]
	v_exp_f32_e32 v72, v72
	v_exp_f32_e32 v73, v73
	v_pk_add_f32 v[14:15], v[14:15], v[54:55]
	v_exp_f32_e32 v56, v56
	v_exp_f32_e32 v57, v57
	v_pk_add_f32 v[14:15], v[14:15], v[72:73]
	v_exp_f32_e32 v74, v74
	v_exp_f32_e32 v75, v75
	v_pk_add_f32 v[14:15], v[14:15], v[56:57]
	v_exp_f32_e32 v58, v58
	v_exp_f32_e32 v59, v59
	v_pk_add_f32 v[14:15], v[14:15], v[74:75]
	v_exp_f32_e32 v76, v76
	v_exp_f32_e32 v77, v77
	v_pk_add_f32 v[14:15], v[14:15], v[58:59]
	v_exp_f32_e32 v60, v60
	v_exp_f32_e32 v61, v61
	v_pk_add_f32 v[14:15], v[14:15], v[76:77]
	v_exp_f32_e32 v78, v78
	v_exp_f32_e32 v79, v79
	v_pk_add_f32 v[14:15], v[14:15], v[60:61]
	v_exp_f32_e32 v62, v62
	v_exp_f32_e32 v63, v63
	v_pk_add_f32 v[14:15], v[14:15], v[78:79]
	v_pk_add_f32 v[14:15], v[14:15], v[62:63]
	s_and_b64 s[90:91], s[90:91], s[70:71]
	v_add_f32_e32 v14, v14, v15
	v_add_f32_e32 v1, v1, v14
	v_cvt_pk_bf16_f32 v64, v64, v65
	v_cvt_pk_bf16_f32 v65, v66, v67
	v_cvt_pk_bf16_f32 v66, v68, v69
	v_cvt_pk_bf16_f32 v67, v70, v71
	v_cvt_pk_bf16_f32 v68, v72, v73
	v_cvt_pk_bf16_f32 v69, v74, v75
	v_cvt_pk_bf16_f32 v70, v76, v77
	v_cvt_pk_bf16_f32 v71, v78, v79
	v_cvt_pk_bf16_f32 v48, v48, v49
	v_cvt_pk_bf16_f32 v49, v50, v51
	v_cvt_pk_bf16_f32 v50, v52, v53
	v_cvt_pk_bf16_f32 v51, v54, v55
	v_cvt_pk_bf16_f32 v52, v56, v57
	v_cvt_pk_bf16_f32 v53, v58, v59
	v_cvt_pk_bf16_f32 v54, v60, v61
	v_cvt_pk_bf16_f32 v55, v62, v63
	s_waitcnt lgkmcnt(14)
	v_mfma_f32_32x32x16_bf16 v[16:31], v[88:91], v[64:67], v[16:31]
	s_waitcnt lgkmcnt(6)
	v_mfma_f32_32x32x16_bf16 v[32:47], v[96:99], v[64:67], v[32:47]
	v_mfma_f32_32x32x16_bf16 v[16:31], v[80:83], v[68:71], v[16:31]
	s_waitcnt lgkmcnt(4)
	v_mfma_f32_32x32x16_bf16 v[32:47], v[92:95], v[68:71], v[32:47]
	v_mfma_f32_32x32x16_bf16 v[16:31], v[6:9], v[48:51], v[16:31]
	s_waitcnt lgkmcnt(2)
	v_mfma_f32_32x32x16_bf16 v[32:47], v[84:87], v[48:51], v[32:47]
	v_mfma_f32_32x32x16_bf16 v[16:31], v[2:5], v[52:55], v[16:31]
	s_waitcnt lgkmcnt(0)
	v_mfma_f32_32x32x16_bf16 v[32:47], v[10:13], v[52:55], v[32:47]
	s_flbit_i32_b64 s70, s[72:73]
	s_xor_b32 s76, s70, 63
	s_lshl_b64 s[70:71], 1, s76
	s_andn2_b64 s[70:71], s[72:73], s[70:71]
	s_cmp_lg_u64 s[72:73], 0
	s_cselect_b32 s72, s76, -1
	s_addk_i32 s84, 0x4000
	s_cmp_lt_i32 s1, 0
	s_cbranch_scc1 .LBB0_622
	s_mov_b32 s77, s0
	s_mov_b32 s0, s72
	s_mov_b64 s[72:73], s[70:71]
	s_mov_b32 s76, s1
	s_branch .LBB0_612
